# v78 + selected-branch tile loop: next group's mask words requested ahead of the loop barrier, loop-back edge enters behind the read
# speedup vs baseline: 1.0049x; 1.0015x over previous
.Lslc_nm_head2:
	s_add_i32 s33, s77, -3
	s_and_b32 s76, s33, 4
	s_add_i32 s5, s77, 4
	v_readlane_b32 s32, v252, 28
	s_cmp_eq_u32 s76, 0
	s_cselect_b32 s0, 0x10000, 0
	s_add_i32 s32, s32, s0
	s_add_i32 s0, s77, 1
	s_cmp_gt_u32 s0, s83
	s_cbranch_scc1 .Lslc_nm_dma_skip_0
	s_add_u32 s80, s74, 0x1fb08000
	s_addc_u32 s81, s75, 0
	s_add_i32 m0, s32, 0x0
	s_nop 0
	global_load_lds_dwordx4 v150, s[80:81]
	s_add_u32 s0, s74, 0x20b08000
	s_addc_u32 s1, s75, 0
	s_add_i32 m0, s32, 0x8000
	s_nop 0
	global_load_lds_dwordx4 v152, s[0:1]

.LBB0_2115:
	s_add_i32 s0, s5, -3
	s_add_u32 s74, s74, 0x8000
	s_addc_u32 s75, s75, 0
	s_lshr_b32 s1, s0, 3
	s_and_b32 s1, s1, 0x1ffffffc
	v_add_u32_e32 v1, s1, v225
	ds_read2_b32 v[4:5], v1 offset1:16
	s_cmp_gt_u32 s0, s83
	s_waitcnt vmcnt(0)
	s_barrier
	s_cbranch_scc1 .LBB0_2117
	s_mov_b32 s77, s5
	s_branch .Lslc_nm_head2
